# SwiGLU epilogues: packed f32 multiplies/adds split into scalar pairs
# baseline (speedup 1.0000x reference)
.Lalign_p3:
	s_waitcnt vmcnt(7)
	v_mul_f32_e32 v182, v88, v170
	v_mul_f32_e32 v183, v89, v170
	v_mul_f32_e32 v186, v84, v170
	v_mul_f32_e32 v187, v85, v170
	v_mul_f32_e32 v180, v90, v170
	v_mul_f32_e32 v181, v91, v170
	v_mul_f32_e32 v184, v86, v170
	v_mul_f32_e32 v185, v87, v170
	v_mul_f32_e32 v188, v80, v170
	v_mul_f32_e32 v189, v81, v170
	v_mul_f32_e32 v190, v82, v170
	v_mul_f32_e32 v191, v83, v170
	v_mul_f32_e32 v140, v182, v140
	v_mul_f32_e32 v141, v183, v141
	v_mul_f32_e32 v136, v186, v136
	v_mul_f32_e32 v137, v187, v137
	v_mul_f32_e32 v192, v76, v170
	v_mul_f32_e32 v193, v77, v170
	v_mul_f32_e32 v171, v79, v170
	v_mul_f32_e32 v170, v78, v170
	v_mul_f32_e32 v142, v180, v142
	v_mul_f32_e32 v143, v181, v143
	v_mul_f32_e32 v138, v184, v138
	v_mul_f32_e32 v139, v185, v139
	v_mul_f32_e32 v134, v190, v134
	v_mul_f32_e32 v135, v191, v135
	v_mul_f32_e32 v132, v188, v132
	v_mul_f32_e32 v133, v189, v133
	v_mul_f32_e32 v180, s12, v140
	v_mul_f32_e32 v181, s12, v141
	v_mul_f32_e32 v184, s12, v136
	v_mul_f32_e32 v185, s12, v137
	v_mul_f32_e32 v170, v170, v174
	v_mul_f32_e32 v171, v171, v175
	v_mul_f32_e32 v174, s12, v142
	v_mul_f32_e32 v175, s12, v143
	v_mul_f32_e32 v132, v140, v132
	v_mul_f32_e32 v133, v141, v133
	v_mul_f32_e32 v134, v142, v134
	v_mul_f32_e32 v135, v143, v135
	v_exp_f32_e32 v140, v180
	v_exp_f32_e32 v142, v184
	v_exp_f32_e32 v141, v181
	v_exp_f32_e32 v143, v185
	v_mul_f32_e32 v172, v192, v172
	v_mul_f32_e32 v173, v193, v173
	v_mul_f32_e32 v182, s12, v138
	v_mul_f32_e32 v183, s12, v139
	v_mul_f32_e32 v136, v136, v172
	v_mul_f32_e32 v137, v137, v173
	v_mul_f32_e32 v138, v138, v170
	v_mul_f32_e32 v139, v139, v171
	v_exp_f32_e32 v170, v174
	v_exp_f32_e32 v171, v175
	v_exp_f32_e32 v172, v182
	v_exp_f32_e32 v173, v183
	v_add_f32_e32 v140, 1.0, v140
	v_add_f32_e32 v141, 1.0, v141
	v_add_f32_e32 v142, 1.0, v142
	v_add_f32_e32 v143, 1.0, v143
	v_rcp_f32_e32 v140, v140
	v_rcp_f32_e32 v142, v142
	v_rcp_f32_e32 v141, v141
	v_rcp_f32_e32 v143, v143
	v_add_f32_e32 v170, 1.0, v170
	v_add_f32_e32 v171, 1.0, v171
	v_add_f32_e32 v172, 1.0, v172
	v_add_f32_e32 v173, 1.0, v173
	v_rcp_f32_e32 v170, v170
	v_rcp_f32_e32 v172, v172
	v_rcp_f32_e32 v171, v171
	v_rcp_f32_e32 v173, v173
	v_mul_f32_e32 v132, v132, v140
	v_mul_f32_e32 v133, v133, v141
	v_mul_f32_e32 v136, v136, v142
	v_mul_f32_e32 v137, v137, v143
	v_cvt_pk_fp8_f32 v176, v132, v133
	v_cvt_pk_fp8_f32 v177, v136, v137
	v_mul_f32_e32 v132, v134, v170
	v_mul_f32_e32 v133, v135, v171
	v_mul_f32_e32 v134, v138, v172
	v_mul_f32_e32 v135, v139, v173
	v_cvt_pk_fp8_f32 v176, v132, v133 op_sel:[0,0,1]
	v_cvt_pk_fp8_f32 v177, v134, v135 op_sel:[0,0,1]
	v_lshl_add_u64 v[132:133], v[168:169], 0, v[128:129]
	v_or_b32_e32 v136, 32, v160
	global_store_dwordx2 v[132:133], v[176:177], off
	v_mov_b32_e32 v134, 0
	v_mov_b32_e32 v135, 0
	v_mad_i64_i32 v[138:139], s[24:25], v178, s48, v[130:131]
	v_ashrrev_i32_e32 v137, 31, v136
	v_cvt_f32_i32_e32 v56, v56
	v_cvt_f32_i32_e32 v63, v63
	v_cvt_f32_i32_e32 v62, v62
	v_cvt_f32_i32_e32 v59, v59
	v_cvt_f32_i32_e32 v58, v58
	v_cvt_f32_i32_e32 v49, v49
	v_cvt_f32_i32_e32 v48, v48
	v_cvt_f32_i32_e32 v51, v51
	v_cvt_f32_i32_e32 v50, v50
	v_cvt_f32_i32_e32 v53, v53
	v_cvt_f32_i32_e32 v52, v52
	v_cvt_f32_i32_e32 v55, v55
	v_cvt_f32_i32_e32 v54, v54
	v_cvt_f32_i32_e32 v45, v45
	v_cvt_f32_i32_e32 v44, v44
	v_cvt_f32_i32_e32 v41, v41
	v_cvt_f32_i32_e32 v40, v40
	v_cvt_f32_i32_e32 v47, v47
	v_cvt_f32_i32_e32 v46, v46
	v_cvt_f32_i32_e32 v43, v43
	v_cvt_f32_i32_e32 v42, v42
	v_cvt_f32_i32_e32 v33, v33
	v_cvt_f32_i32_e32 v32, v32
	v_cvt_f32_i32_e32 v35, v35
	v_cvt_f32_i32_e32 v34, v34
	v_cvt_f32_i32_e32 v37, v37
	v_cvt_f32_i32_e32 v36, v36
	v_cvt_f32_i32_e32 v39, v39
	v_cvt_f32_i32_e32 v38, v38
	v_cvt_f32_i32_e32 v29, v29
	v_cvt_f32_i32_e32 v28, v28
	v_cvt_f32_i32_e32 v25, v25
	v_cvt_f32_i32_e32 v24, v24
	v_cvt_f32_i32_e32 v31, v31
	v_cvt_f32_i32_e32 v30, v30
	v_cvt_f32_i32_e32 v27, v27
	v_cvt_f32_i32_e32 v26, v26
	v_cvt_f32_i32_e32 v17, v17
	v_cvt_f32_i32_e32 v16, v16
	v_cvt_f32_i32_e32 v19, v19
	v_cvt_f32_i32_e32 v18, v18
	v_cvt_f32_i32_e32 v21, v21
	v_cvt_f32_i32_e32 v20, v20
	v_cvt_f32_i32_e32 v23, v23
	v_cvt_f32_i32_e32 v22, v22
	v_cvt_f32_i32_e32 v13, v13
	v_cvt_f32_i32_e32 v12, v12
	v_cvt_f32_i32_e32 v9, v9
	v_cvt_f32_i32_e32 v8, v8
	v_cvt_f32_i32_e32 v15, v15
	v_cvt_f32_i32_e32 v14, v14
	v_cvt_f32_i32_e32 v11, v11
	v_cvt_f32_i32_e32 v10, v10
	v_cvt_f32_i32_e32 v1, v1
	v_cvt_f32_i32_e32 v0, v0
	v_cvt_f32_i32_e32 v3, v3
	v_cvt_f32_i32_e32 v2, v2
	v_cvt_f32_i32_e32 v5, v5
	v_cvt_f32_i32_e32 v4, v4
	v_cvt_f32_i32_e32 v7, v7
	v_cvt_f32_i32_e32 v6, v6
	s_andn2_b64 vcc, exec, s[0:1]
	s_mov_b64 s[0:1], -1
	s_waitcnt vmcnt(7)
	v_mul_f32_e32 v142, v88, v196
	v_mul_f32_e32 v143, v89, v196
	v_mul_f32_e32 v170, v84, v196
	v_mul_f32_e32 v171, v85, v196
	v_mul_f32_e32 v140, v90, v196
	v_mul_f32_e32 v141, v91, v196
	v_mul_f32_e32 v168, v86, v196
	v_mul_f32_e32 v169, v87, v196
	v_mul_f32_e32 v172, v80, v196
	v_mul_f32_e32 v173, v81, v196
	v_mul_f32_e32 v174, v82, v196
	v_mul_f32_e32 v175, v83, v196
	v_mul_f32_e32 v176, v76, v196
	v_mul_f32_e32 v177, v77, v196
	v_mul_f32_e32 v132, v78, v196
	v_mul_f32_e32 v133, v79, v196
	v_mul_f32_e32 v124, v142, v124
	v_mul_f32_e32 v125, v143, v125
	v_mul_f32_e32 v120, v170, v120
	v_mul_f32_e32 v121, v171, v121
	v_mul_f32_e32 v126, v140, v126
	v_mul_f32_e32 v127, v141, v127
	v_mul_f32_e32 v122, v168, v122
	v_mul_f32_e32 v123, v169, v123
	v_mul_f32_e32 v114, v132, v114
	v_mul_f32_e32 v115, v133, v115
	v_mul_f32_e32 v112, v176, v112
	v_mul_f32_e32 v113, v177, v113
	v_mul_f32_e32 v140, s12, v124
	v_mul_f32_e32 v141, s12, v125
	v_mul_f32_e32 v168, s12, v120
	v_mul_f32_e32 v169, s12, v121
	v_mul_f32_e32 v142, s12, v122
	v_mul_f32_e32 v143, s12, v123
	v_mul_f32_e32 v112, v120, v112
	v_mul_f32_e32 v113, v121, v113
	v_mul_f32_e32 v114, v122, v114
	v_mul_f32_e32 v115, v123, v115
	v_exp_f32_e32 v120, v140
	v_exp_f32_e32 v122, v168
	v_exp_f32_e32 v121, v141
	v_exp_f32_e32 v123, v169
	v_mul_f32_e32 v118, v174, v118
	v_mul_f32_e32 v119, v175, v119
	v_mul_f32_e32 v116, v172, v116
	v_mul_f32_e32 v117, v173, v117
	v_mul_f32_e32 v132, s12, v126
	v_mul_f32_e32 v133, s12, v127
	v_mul_f32_e32 v116, v124, v116
	v_mul_f32_e32 v117, v125, v117
	v_mul_f32_e32 v118, v126, v118
	v_mul_f32_e32 v119, v127, v119
	v_exp_f32_e32 v124, v132
	v_exp_f32_e32 v125, v133
	v_exp_f32_e32 v126, v142
	v_exp_f32_e32 v127, v143
	v_add_f32_e32 v120, 1.0, v120
	v_add_f32_e32 v121, 1.0, v121
	v_add_f32_e32 v122, 1.0, v122
	v_add_f32_e32 v123, 1.0, v123
	v_rcp_f32_e32 v120, v120
	v_rcp_f32_e32 v122, v122
	v_rcp_f32_e32 v121, v121
	v_rcp_f32_e32 v123, v123
	v_add_f32_e32 v124, 1.0, v124
	v_add_f32_e32 v125, 1.0, v125
	v_add_f32_e32 v126, 1.0, v126
	v_add_f32_e32 v127, 1.0, v127
	v_rcp_f32_e32 v124, v124
	v_rcp_f32_e32 v126, v126
	v_rcp_f32_e32 v125, v125
	v_rcp_f32_e32 v127, v127
	v_mul_f32_e32 v116, v116, v120
	v_mul_f32_e32 v117, v117, v121
	v_mul_f32_e32 v112, v112, v122
	v_mul_f32_e32 v113, v113, v123
	v_cvt_pk_fp8_f32 v134, v116, v117
	v_cvt_pk_fp8_f32 v135, v112, v113
	v_mul_f32_e32 v112, v118, v124
	v_mul_f32_e32 v113, v119, v125
	v_mul_f32_e32 v114, v114, v126
	v_mul_f32_e32 v115, v115, v127
	v_cvt_pk_fp8_f32 v134, v112, v113 op_sel:[0,0,1]
	v_cvt_pk_fp8_f32 v135, v114, v115 op_sel:[0,0,1]
	v_lshl_add_u64 v[112:113], v[138:139], 0, v[128:129]
	v_mad_i64_i32 v[118:119], s[24:25], v136, s48, v[130:131]
	global_store_dwordx2 v[112:113], v[134:135], off
	v_mov_b32_e32 v114, 0
	v_mov_b32_e32 v115, 0
	v_or_b32_e32 v116, 48, v160
	v_ashrrev_i32_e32 v117, 31, v116
	s_waitcnt vmcnt(7)
	v_mul_f32_e32 v122, v88, v198
	v_mul_f32_e32 v123, v89, v198
	v_mul_f32_e32 v126, v84, v198
	v_mul_f32_e32 v127, v85, v198
	v_mul_f32_e32 v120, v90, v198
	v_mul_f32_e32 v121, v91, v198
	v_mul_f32_e32 v124, v86, v198
	v_mul_f32_e32 v125, v87, v198
	v_mul_f32_e32 v132, v80, v198
	v_mul_f32_e32 v133, v81, v198
	v_mul_f32_e32 v134, v82, v198
	v_mul_f32_e32 v135, v83, v198
	v_mul_f32_e32 v136, v76, v198
	v_mul_f32_e32 v137, v77, v198
	v_mul_f32_e32 v112, v78, v198
	v_mul_f32_e32 v113, v79, v198
	v_mul_f32_e32 v108, v122, v108
	v_mul_f32_e32 v109, v123, v109
	v_mul_f32_e32 v104, v126, v104
	v_mul_f32_e32 v105, v127, v105
	v_mul_f32_e32 v110, v120, v110
	v_mul_f32_e32 v111, v121, v111
	v_mul_f32_e32 v106, v124, v106
	v_mul_f32_e32 v107, v125, v107
	v_mul_f32_e32 v98, v112, v98
	v_mul_f32_e32 v99, v113, v99
	v_mul_f32_e32 v96, v136, v96
	v_mul_f32_e32 v97, v137, v97
	v_mul_f32_e32 v120, s12, v108
	v_mul_f32_e32 v121, s12, v109
	v_mul_f32_e32 v124, s12, v104
	v_mul_f32_e32 v125, s12, v105
	v_mul_f32_e32 v122, s12, v106
	v_mul_f32_e32 v123, s12, v107
	v_mul_f32_e32 v96, v104, v96
	v_mul_f32_e32 v97, v105, v97
	v_mul_f32_e32 v98, v106, v98
	v_mul_f32_e32 v99, v107, v99
	v_exp_f32_e32 v104, v120
	v_exp_f32_e32 v106, v124
	v_exp_f32_e32 v105, v121
	v_exp_f32_e32 v107, v125
	v_mul_f32_e32 v102, v134, v102
	v_mul_f32_e32 v103, v135, v103
	v_mul_f32_e32 v100, v132, v100
	v_mul_f32_e32 v101, v133, v101
	v_mul_f32_e32 v112, s12, v110
	v_mul_f32_e32 v113, s12, v111
	v_mul_f32_e32 v100, v108, v100
	v_mul_f32_e32 v101, v109, v101
	v_mul_f32_e32 v102, v110, v102
	v_mul_f32_e32 v103, v111, v103
	v_exp_f32_e32 v108, v112
	v_exp_f32_e32 v109, v113
	v_exp_f32_e32 v110, v122
	v_exp_f32_e32 v111, v123
	v_add_f32_e32 v104, 1.0, v104
	v_add_f32_e32 v105, 1.0, v105
	v_add_f32_e32 v106, 1.0, v106
	v_add_f32_e32 v107, 1.0, v107
	v_rcp_f32_e32 v104, v104
	v_rcp_f32_e32 v106, v106
	v_rcp_f32_e32 v105, v105
	v_rcp_f32_e32 v107, v107
	v_add_f32_e32 v108, 1.0, v108
	v_add_f32_e32 v109, 1.0, v109
	v_add_f32_e32 v110, 1.0, v110
	v_add_f32_e32 v111, 1.0, v111
	v_rcp_f32_e32 v108, v108
	v_rcp_f32_e32 v110, v110
	v_rcp_f32_e32 v109, v109
	v_rcp_f32_e32 v111, v111
	v_mul_f32_e32 v100, v100, v104
	v_mul_f32_e32 v101, v101, v105
	v_mul_f32_e32 v96, v96, v106
	v_mul_f32_e32 v97, v97, v107
	v_cvt_pk_fp8_f32 v114, v100, v101
	v_cvt_pk_fp8_f32 v115, v96, v97
	v_mul_f32_e32 v96, v102, v108
	v_mul_f32_e32 v97, v103, v109
	v_mul_f32_e32 v98, v98, v110
	v_mul_f32_e32 v99, v99, v111
	v_cvt_pk_fp8_f32 v114, v96, v97 op_sel:[0,0,1]
	v_cvt_pk_fp8_f32 v115, v98, v99 op_sel:[0,0,1]
	v_lshl_add_u64 v[96:97], v[118:119], 0, v[128:129]
	global_store_dwordx2 v[96:97], v[114:115], off
	v_mov_b32_e32 v98, 0
	v_mov_b32_e32 v99, 0
	s_waitcnt vmcnt(7)
	v_mul_f32_e32 v102, v88, v200
	v_mul_f32_e32 v103, v89, v200
	v_mul_f32_e32 v106, v84, v200
	v_mul_f32_e32 v107, v85, v200
	v_mul_f32_e32 v100, v90, v200
	v_mul_f32_e32 v101, v91, v200
	v_mul_f32_e32 v104, v86, v200
	v_mul_f32_e32 v105, v87, v200
	v_mul_f32_e32 v108, v80, v200
	v_mul_f32_e32 v109, v81, v200
	v_mul_f32_e32 v110, v82, v200
	v_mul_f32_e32 v111, v83, v200
	v_mul_f32_e32 v112, v76, v200
	v_mul_f32_e32 v113, v77, v200
	v_mul_f32_e32 v96, v78, v200
	v_mul_f32_e32 v97, v79, v200
	v_mul_f32_e32 v92, v102, v92
	v_mul_f32_e32 v93, v103, v93
	v_mul_f32_e32 v72, v106, v72
	v_mul_f32_e32 v73, v107, v73
	v_mul_f32_e32 v94, v100, v94
	v_mul_f32_e32 v95, v101, v95
	v_mul_f32_e32 v74, v104, v74
	v_mul_f32_e32 v75, v105, v75
	v_mul_f32_e32 v66, v96, v66
	v_mul_f32_e32 v67, v97, v67
	v_mul_f32_e32 v64, v112, v64
	v_mul_f32_e32 v65, v113, v65
	v_mul_f32_e32 v100, s12, v92
	v_mul_f32_e32 v101, s12, v93
	v_mul_f32_e32 v104, s12, v72
	v_mul_f32_e32 v105, s12, v73
	v_mul_f32_e32 v102, s12, v74
	v_mul_f32_e32 v103, s12, v75
	v_mul_f32_e32 v64, v72, v64
	v_mul_f32_e32 v65, v73, v65
	v_mul_f32_e32 v66, v74, v66
	v_mul_f32_e32 v67, v75, v67
	v_exp_f32_e32 v72, v100
	v_exp_f32_e32 v74, v104
	v_exp_f32_e32 v73, v101
	v_exp_f32_e32 v75, v105
	v_mul_f32_e32 v70, v110, v70
	v_mul_f32_e32 v71, v111, v71
	v_mul_f32_e32 v68, v108, v68
	v_mul_f32_e32 v69, v109, v69
	v_mul_f32_e32 v96, s12, v94
	v_mul_f32_e32 v97, s12, v95
	v_mul_f32_e32 v68, v92, v68
	v_mul_f32_e32 v69, v93, v69
	v_mul_f32_e32 v70, v94, v70
	v_mul_f32_e32 v71, v95, v71
	v_exp_f32_e32 v92, v96
	v_exp_f32_e32 v93, v97
	v_exp_f32_e32 v94, v102
	v_exp_f32_e32 v95, v103
	v_add_f32_e32 v72, 1.0, v72
	v_add_f32_e32 v73, 1.0, v73
	v_add_f32_e32 v74, 1.0, v74
	v_add_f32_e32 v75, 1.0, v75
	v_rcp_f32_e32 v72, v72
	v_rcp_f32_e32 v74, v74
	v_rcp_f32_e32 v73, v73
	v_rcp_f32_e32 v75, v75
	v_add_f32_e32 v92, 1.0, v92
	v_add_f32_e32 v93, 1.0, v93
	v_add_f32_e32 v94, 1.0, v94
	v_add_f32_e32 v95, 1.0, v95
	v_rcp_f32_e32 v92, v92
	v_rcp_f32_e32 v94, v94
	v_rcp_f32_e32 v93, v93
	v_rcp_f32_e32 v95, v95
	v_mul_f32_e32 v68, v68, v72
	v_mul_f32_e32 v69, v69, v73
	v_mul_f32_e32 v64, v64, v74
	v_mul_f32_e32 v65, v65, v75
	v_cvt_pk_fp8_f32 v98, v68, v69
	v_cvt_pk_fp8_f32 v99, v64, v65
	v_mul_f32_e32 v64, v70, v92
	v_mul_f32_e32 v65, v71, v93
	v_mul_f32_e32 v66, v66, v94
	v_mul_f32_e32 v67, v67, v95
	v_cvt_pk_fp8_f32 v98, v64, v65 op_sel:[0,0,1]
	v_cvt_pk_fp8_f32 v99, v66, v67 op_sel:[0,0,1]
	v_mad_i64_i32 v[64:65], s[24:25], v116, s48, v[130:131]
	v_lshl_add_u64 v[64:65], v[64:65], 0, v[128:129]
	global_store_dwordx2 v[64:65], v[98:99], off
	v_mov_b32_e32 v66, 0
	v_mov_b32_e32 v67, 0
	v_add_u32_e32 v98, 0x80, v160
	s_waitcnt vmcnt(7)
	v_mul_f32_e32 v70, v88, v202
	v_mul_f32_e32 v71, v89, v202
	v_mul_f32_e32 v74, v84, v202
	v_mul_f32_e32 v75, v85, v202
	v_mul_f32_e32 v68, v90, v202
	v_mul_f32_e32 v69, v91, v202
	v_mul_f32_e32 v72, v86, v202
	v_mul_f32_e32 v73, v87, v202
	v_mul_f32_e32 v92, v80, v202
	v_mul_f32_e32 v93, v81, v202
	v_mul_f32_e32 v94, v82, v202
	v_mul_f32_e32 v95, v83, v202
	v_mul_f32_e32 v96, v76, v202
	v_mul_f32_e32 v97, v77, v202
	v_mul_f32_e32 v64, v78, v202
	v_mul_f32_e32 v65, v79, v202
	v_mul_f32_e32 v60, v70, v60
	v_mul_f32_e32 v61, v71, v61
	v_mul_f32_e32 v56, v74, v56
	v_mul_f32_e32 v57, v75, v57
	v_mul_f32_e32 v62, v68, v62
	v_mul_f32_e32 v63, v69, v63
	v_mul_f32_e32 v58, v72, v58
	v_mul_f32_e32 v59, v73, v59
	v_mul_f32_e32 v50, v64, v50
	v_mul_f32_e32 v51, v65, v51
	v_mul_f32_e32 v48, v96, v48
	v_mul_f32_e32 v49, v97, v49
	v_mul_f32_e32 v68, s12, v60
	v_mul_f32_e32 v69, s12, v61
	v_mul_f32_e32 v72, s12, v56
	v_mul_f32_e32 v73, s12, v57
	v_mul_f32_e32 v70, s12, v58
	v_mul_f32_e32 v71, s12, v59
	v_mul_f32_e32 v48, v56, v48
	v_mul_f32_e32 v49, v57, v49
	v_mul_f32_e32 v50, v58, v50
	v_mul_f32_e32 v51, v59, v51
	v_exp_f32_e32 v56, v68
	v_exp_f32_e32 v58, v72
	v_exp_f32_e32 v57, v69
	v_exp_f32_e32 v59, v73
	v_mul_f32_e32 v54, v94, v54
	v_mul_f32_e32 v55, v95, v55
	v_mul_f32_e32 v52, v92, v52
	v_mul_f32_e32 v53, v93, v53
	v_mul_f32_e32 v64, s12, v62
	v_mul_f32_e32 v65, s12, v63
	v_mul_f32_e32 v52, v60, v52
	v_mul_f32_e32 v53, v61, v53
	v_mul_f32_e32 v54, v62, v54
	v_mul_f32_e32 v55, v63, v55
	v_exp_f32_e32 v60, v64
	v_exp_f32_e32 v61, v65
	v_exp_f32_e32 v62, v70
	v_exp_f32_e32 v63, v71
	v_add_f32_e32 v56, 1.0, v56
	v_add_f32_e32 v57, 1.0, v57
	v_add_f32_e32 v58, 1.0, v58
	v_add_f32_e32 v59, 1.0, v59
	v_rcp_f32_e32 v56, v56
	v_rcp_f32_e32 v58, v58
	v_rcp_f32_e32 v57, v57
	v_rcp_f32_e32 v59, v59
	v_add_f32_e32 v60, 1.0, v60
	v_add_f32_e32 v61, 1.0, v61
	v_add_f32_e32 v62, 1.0, v62
	v_add_f32_e32 v63, 1.0, v63
	v_rcp_f32_e32 v60, v60
	v_rcp_f32_e32 v62, v62
	v_rcp_f32_e32 v61, v61
	v_rcp_f32_e32 v63, v63
	v_mul_f32_e32 v52, v52, v56
	v_mul_f32_e32 v53, v53, v57
	v_mul_f32_e32 v48, v48, v58
	v_mul_f32_e32 v49, v49, v59
	v_cvt_pk_fp8_f32 v66, v52, v53
	v_cvt_pk_fp8_f32 v67, v48, v49
	v_mul_f32_e32 v48, v54, v60
	v_mul_f32_e32 v49, v55, v61
	v_mul_f32_e32 v50, v50, v62
	v_mul_f32_e32 v51, v51, v63
	v_cvt_pk_fp8_f32 v66, v48, v49 op_sel:[0,0,1]
	v_cvt_pk_fp8_f32 v67, v50, v51 op_sel:[0,0,1]
	v_mad_i64_i32 v[48:49], s[24:25], v98, s48, v[130:131]
	v_lshl_add_u64 v[48:49], v[48:49], 0, v[128:129]
	global_store_dwordx2 v[48:49], v[66:67], off
	v_mov_b32_e32 v50, 0
	v_mov_b32_e32 v51, 0
	v_add_u32_e32 v66, 0x90, v160
	s_waitcnt vmcnt(7)
	v_mul_f32_e32 v54, v88, v204
	v_mul_f32_e32 v55, v89, v204
	v_mul_f32_e32 v58, v84, v204
	v_mul_f32_e32 v59, v85, v204
	v_mul_f32_e32 v52, v90, v204
	v_mul_f32_e32 v53, v91, v204
	v_mul_f32_e32 v56, v86, v204
	v_mul_f32_e32 v57, v87, v204
	v_mul_f32_e32 v60, v80, v204
	v_mul_f32_e32 v61, v81, v204
	v_mul_f32_e32 v62, v82, v204
	v_mul_f32_e32 v63, v83, v204
	v_mul_f32_e32 v64, v76, v204
	v_mul_f32_e32 v65, v77, v204
	v_mul_f32_e32 v48, v78, v204
	v_mul_f32_e32 v49, v79, v204
	v_mul_f32_e32 v44, v54, v44
	v_mul_f32_e32 v45, v55, v45
	v_mul_f32_e32 v40, v58, v40
	v_mul_f32_e32 v41, v59, v41
	v_mul_f32_e32 v46, v52, v46
	v_mul_f32_e32 v47, v53, v47
	v_mul_f32_e32 v42, v56, v42
	v_mul_f32_e32 v43, v57, v43
	v_mul_f32_e32 v34, v48, v34
	v_mul_f32_e32 v35, v49, v35
	v_mul_f32_e32 v32, v64, v32
	v_mul_f32_e32 v33, v65, v33
	v_mul_f32_e32 v52, s12, v44
	v_mul_f32_e32 v53, s12, v45
	v_mul_f32_e32 v56, s12, v40
	v_mul_f32_e32 v57, s12, v41
	v_mul_f32_e32 v54, s12, v42
	v_mul_f32_e32 v55, s12, v43
	v_mul_f32_e32 v32, v40, v32
	v_mul_f32_e32 v33, v41, v33
	v_mul_f32_e32 v34, v42, v34
	v_mul_f32_e32 v35, v43, v35
	v_exp_f32_e32 v40, v52
	v_exp_f32_e32 v42, v56
	v_exp_f32_e32 v41, v53
	v_exp_f32_e32 v43, v57
	v_mul_f32_e32 v38, v62, v38
	v_mul_f32_e32 v39, v63, v39
	v_mul_f32_e32 v36, v60, v36
	v_mul_f32_e32 v37, v61, v37
	v_mul_f32_e32 v48, s12, v46
	v_mul_f32_e32 v49, s12, v47
	v_mul_f32_e32 v36, v44, v36
	v_mul_f32_e32 v37, v45, v37
	v_mul_f32_e32 v38, v46, v38
	v_mul_f32_e32 v39, v47, v39
	v_exp_f32_e32 v44, v48
	v_exp_f32_e32 v45, v49
	v_exp_f32_e32 v46, v54
	v_exp_f32_e32 v47, v55
	v_add_f32_e32 v40, 1.0, v40
	v_add_f32_e32 v41, 1.0, v41
	v_add_f32_e32 v42, 1.0, v42
	v_add_f32_e32 v43, 1.0, v43
	v_rcp_f32_e32 v40, v40
	v_rcp_f32_e32 v42, v42
	v_rcp_f32_e32 v41, v41
	v_rcp_f32_e32 v43, v43
	v_add_f32_e32 v44, 1.0, v44
	v_add_f32_e32 v45, 1.0, v45
	v_add_f32_e32 v46, 1.0, v46
	v_add_f32_e32 v47, 1.0, v47
	v_rcp_f32_e32 v44, v44
	v_rcp_f32_e32 v46, v46
	v_rcp_f32_e32 v45, v45
	v_rcp_f32_e32 v47, v47
	v_mul_f32_e32 v36, v36, v40
	v_mul_f32_e32 v37, v37, v41
	v_mul_f32_e32 v32, v32, v42
	v_mul_f32_e32 v33, v33, v43
	v_cvt_pk_fp8_f32 v50, v36, v37
	v_cvt_pk_fp8_f32 v51, v32, v33
	v_mul_f32_e32 v32, v38, v44
	v_mul_f32_e32 v33, v39, v45
	v_mul_f32_e32 v34, v34, v46
	v_mul_f32_e32 v35, v35, v47
	v_cvt_pk_fp8_f32 v50, v32, v33 op_sel:[0,0,1]
	v_cvt_pk_fp8_f32 v51, v34, v35 op_sel:[0,0,1]
	v_mad_i64_i32 v[32:33], s[24:25], v66, s48, v[130:131]
	v_lshl_add_u64 v[32:33], v[32:33], 0, v[128:129]
	global_store_dwordx2 v[32:33], v[50:51], off
	v_mov_b32_e32 v34, 0
	v_mov_b32_e32 v35, 0
	v_add_u32_e32 v50, 0xa0, v160
	s_waitcnt vmcnt(7)
	v_mul_f32_e32 v38, v88, v206
	v_mul_f32_e32 v39, v89, v206
	v_mul_f32_e32 v42, v84, v206
	v_mul_f32_e32 v43, v85, v206
	v_mul_f32_e32 v36, v90, v206
	v_mul_f32_e32 v37, v91, v206
	v_mul_f32_e32 v40, v86, v206
	v_mul_f32_e32 v41, v87, v206
	v_mul_f32_e32 v44, v80, v206
	v_mul_f32_e32 v45, v81, v206
	v_mul_f32_e32 v46, v82, v206
	v_mul_f32_e32 v47, v83, v206
	v_mul_f32_e32 v48, v76, v206
	v_mul_f32_e32 v49, v77, v206
	v_mul_f32_e32 v32, v78, v206
	v_mul_f32_e32 v33, v79, v206
	v_mul_f32_e32 v28, v38, v28
	v_mul_f32_e32 v29, v39, v29
	v_mul_f32_e32 v24, v42, v24
	v_mul_f32_e32 v25, v43, v25
	v_mul_f32_e32 v30, v36, v30
	v_mul_f32_e32 v31, v37, v31
	v_mul_f32_e32 v26, v40, v26
	v_mul_f32_e32 v27, v41, v27
	v_mul_f32_e32 v18, v32, v18
	v_mul_f32_e32 v19, v33, v19
	v_mul_f32_e32 v16, v48, v16
	v_mul_f32_e32 v17, v49, v17
	v_mul_f32_e32 v36, s12, v28
	v_mul_f32_e32 v37, s12, v29
	v_mul_f32_e32 v40, s12, v24
	v_mul_f32_e32 v41, s12, v25
	v_mul_f32_e32 v38, s12, v26
	v_mul_f32_e32 v39, s12, v27
	v_mul_f32_e32 v16, v24, v16
	v_mul_f32_e32 v17, v25, v17
	v_mul_f32_e32 v18, v26, v18
	v_mul_f32_e32 v19, v27, v19
	v_exp_f32_e32 v24, v36
	v_exp_f32_e32 v26, v40
	v_exp_f32_e32 v25, v37
	v_exp_f32_e32 v27, v41
	v_mul_f32_e32 v22, v46, v22
	v_mul_f32_e32 v23, v47, v23
	v_mul_f32_e32 v20, v44, v20
	v_mul_f32_e32 v21, v45, v21
	v_mul_f32_e32 v32, s12, v30
	v_mul_f32_e32 v33, s12, v31
	v_mul_f32_e32 v20, v28, v20
	v_mul_f32_e32 v21, v29, v21
	v_mul_f32_e32 v22, v30, v22
	v_mul_f32_e32 v23, v31, v23
	v_exp_f32_e32 v28, v32
	v_exp_f32_e32 v29, v33
	v_exp_f32_e32 v30, v38
	v_exp_f32_e32 v31, v39
	v_add_f32_e32 v24, 1.0, v24
	v_add_f32_e32 v25, 1.0, v25
	v_add_f32_e32 v26, 1.0, v26
	v_add_f32_e32 v27, 1.0, v27
	v_rcp_f32_e32 v24, v24
	v_rcp_f32_e32 v26, v26
	v_rcp_f32_e32 v25, v25
	v_rcp_f32_e32 v27, v27
	v_add_f32_e32 v28, 1.0, v28
	v_add_f32_e32 v29, 1.0, v29
	v_add_f32_e32 v30, 1.0, v30
	v_add_f32_e32 v31, 1.0, v31
	v_rcp_f32_e32 v28, v28
	v_rcp_f32_e32 v30, v30
	v_rcp_f32_e32 v29, v29
	v_rcp_f32_e32 v31, v31
	v_mul_f32_e32 v20, v20, v24
	v_mul_f32_e32 v21, v21, v25
	v_mul_f32_e32 v16, v16, v26
	v_mul_f32_e32 v17, v17, v27
	v_cvt_pk_fp8_f32 v34, v20, v21
	v_cvt_pk_fp8_f32 v35, v16, v17
	v_mul_f32_e32 v16, v22, v28
	v_mul_f32_e32 v17, v23, v29
	v_mul_f32_e32 v18, v18, v30
	v_mul_f32_e32 v19, v19, v31
	v_cvt_pk_fp8_f32 v34, v16, v17 op_sel:[0,0,1]
	v_cvt_pk_fp8_f32 v35, v18, v19 op_sel:[0,0,1]
	v_mad_i64_i32 v[16:17], s[24:25], v50, s48, v[130:131]
	v_lshl_add_u64 v[16:17], v[16:17], 0, v[128:129]
	global_store_dwordx2 v[16:17], v[34:35], off
	v_mov_b32_e32 v18, 0
	v_mov_b32_e32 v19, 0
	v_add_u32_e32 v34, 0xb0, v160
	s_waitcnt vmcnt(7)
	v_mul_f32_e32 v22, v88, v208
	v_mul_f32_e32 v23, v89, v208
	v_mul_f32_e32 v26, v84, v208
	v_mul_f32_e32 v27, v85, v208
	v_mul_f32_e32 v20, v90, v208
	v_mul_f32_e32 v21, v91, v208
	v_mul_f32_e32 v24, v86, v208
	v_mul_f32_e32 v25, v87, v208
	v_mul_f32_e32 v28, v80, v208
	v_mul_f32_e32 v29, v81, v208
	v_mul_f32_e32 v30, v82, v208
	v_mul_f32_e32 v31, v83, v208
	v_mul_f32_e32 v32, v76, v208
	v_mul_f32_e32 v33, v77, v208
	v_mul_f32_e32 v16, v78, v208
	v_mul_f32_e32 v17, v79, v208
	v_mul_f32_e32 v12, v22, v12
	v_mul_f32_e32 v13, v23, v13
	v_mul_f32_e32 v8, v26, v8
	v_mul_f32_e32 v9, v27, v9
	v_mul_f32_e32 v14, v20, v14
	v_mul_f32_e32 v15, v21, v15
	v_mul_f32_e32 v10, v24, v10
	v_mul_f32_e32 v11, v25, v11
	v_mul_f32_e32 v2, v16, v2
	v_mul_f32_e32 v3, v17, v3
	v_mul_f32_e32 v0, v32, v0
	v_mul_f32_e32 v1, v33, v1
	v_mul_f32_e32 v20, s12, v12
	v_mul_f32_e32 v21, s12, v13
	v_mul_f32_e32 v24, s12, v8
	v_mul_f32_e32 v25, s12, v9
	v_mul_f32_e32 v22, s12, v10
	v_mul_f32_e32 v23, s12, v11
	v_mul_f32_e32 v0, v8, v0
	v_mul_f32_e32 v1, v9, v1
	v_mul_f32_e32 v2, v10, v2
	v_mul_f32_e32 v3, v11, v3
	v_exp_f32_e32 v8, v20
	v_exp_f32_e32 v10, v24
	v_exp_f32_e32 v9, v21
	v_exp_f32_e32 v11, v25
	v_mul_f32_e32 v6, v30, v6
	v_mul_f32_e32 v7, v31, v7
	v_mul_f32_e32 v4, v28, v4
	v_mul_f32_e32 v5, v29, v5
	v_mul_f32_e32 v16, s12, v14
	v_mul_f32_e32 v17, s12, v15
	v_mul_f32_e32 v4, v12, v4
	v_mul_f32_e32 v5, v13, v5
	v_mul_f32_e32 v6, v14, v6
	v_mul_f32_e32 v7, v15, v7
	v_exp_f32_e32 v12, v16
	v_exp_f32_e32 v13, v17
	v_exp_f32_e32 v14, v22
	v_exp_f32_e32 v15, v23
	v_add_f32_e32 v8, 1.0, v8
	v_add_f32_e32 v9, 1.0, v9
	v_add_f32_e32 v10, 1.0, v10
	v_add_f32_e32 v11, 1.0, v11
	v_rcp_f32_e32 v8, v8
	v_rcp_f32_e32 v10, v10
	v_rcp_f32_e32 v9, v9
	v_rcp_f32_e32 v11, v11
	v_add_f32_e32 v12, 1.0, v12
	v_add_f32_e32 v13, 1.0, v13
	v_add_f32_e32 v14, 1.0, v14
	v_add_f32_e32 v15, 1.0, v15
	v_rcp_f32_e32 v12, v12
	v_rcp_f32_e32 v14, v14
	v_rcp_f32_e32 v13, v13
	v_rcp_f32_e32 v15, v15
	v_mul_f32_e32 v4, v4, v8
	v_mul_f32_e32 v5, v5, v9
	v_mul_f32_e32 v0, v0, v10
	v_mul_f32_e32 v1, v1, v11
	v_cvt_pk_fp8_f32 v18, v4, v5
	v_cvt_pk_fp8_f32 v19, v0, v1
	v_mul_f32_e32 v0, v6, v12
	v_mul_f32_e32 v1, v7, v13
	v_mul_f32_e32 v2, v2, v14
	v_mul_f32_e32 v3, v3, v15
	v_cvt_pk_fp8_f32 v18, v0, v1 op_sel:[0,0,1]
	v_cvt_pk_fp8_f32 v19, v2, v3 op_sel:[0,0,1]
	v_mad_i64_i32 v[0:1], s[24:25], v34, s48, v[130:131]
	v_lshl_add_u64 v[0:1], v[0:1], 0, v[128:129]
	global_store_dwordx2 v[0:1], v[18:19], off
	s_cbranch_vccnz .LBB0_490
	s_andn2_b64 vcc, exec, s[4:5]
	s_cbranch_vccnz .LBB0_489
	s_barrier
	s_branch .LBB0_489

.Lalign_p12:
	s_waitcnt vmcnt(7)
	v_mul_f32_e32 v180, v88, v168
	v_mul_f32_e32 v181, v89, v168
	v_mul_f32_e32 v184, v84, v168
	v_mul_f32_e32 v185, v85, v168
	v_mul_f32_e32 v178, v90, v168
	v_mul_f32_e32 v179, v91, v168
	v_mul_f32_e32 v182, v86, v168
	v_mul_f32_e32 v183, v87, v168
	v_mul_f32_e32 v186, v80, v168
	v_mul_f32_e32 v187, v81, v168
	v_mul_f32_e32 v188, v82, v168
	v_mul_f32_e32 v189, v83, v168
	v_mul_f32_e32 v140, v180, v140
	v_mul_f32_e32 v141, v181, v141
	v_mul_f32_e32 v136, v184, v136
	v_mul_f32_e32 v137, v185, v137
	v_mul_f32_e32 v190, v76, v168
	v_mul_f32_e32 v191, v77, v168
	v_mul_f32_e32 v169, v79, v168
	v_mul_f32_e32 v168, v78, v168
	v_mul_f32_e32 v142, v178, v142
	v_mul_f32_e32 v143, v179, v143
	v_mul_f32_e32 v138, v182, v138
	v_mul_f32_e32 v139, v183, v139
	v_mul_f32_e32 v134, v188, v134
	v_mul_f32_e32 v135, v189, v135
	v_mul_f32_e32 v132, v186, v132
	v_mul_f32_e32 v133, v187, v133
	v_mul_f32_e32 v178, s14, v140
	v_mul_f32_e32 v179, s14, v141
	v_mul_f32_e32 v182, s14, v136
	v_mul_f32_e32 v183, s14, v137
	v_mul_f32_e32 v168, v168, v172
	v_mul_f32_e32 v169, v169, v173
	v_mul_f32_e32 v172, s14, v142
	v_mul_f32_e32 v173, s14, v143
	v_mul_f32_e32 v132, v140, v132
	v_mul_f32_e32 v133, v141, v133
	v_mul_f32_e32 v134, v142, v134
	v_mul_f32_e32 v135, v143, v135
	v_exp_f32_e32 v140, v178
	v_exp_f32_e32 v142, v182
	v_exp_f32_e32 v141, v179
	v_exp_f32_e32 v143, v183
	v_mul_f32_e32 v170, v190, v170
	v_mul_f32_e32 v171, v191, v171
	v_mul_f32_e32 v180, s14, v138
	v_mul_f32_e32 v181, s14, v139
	v_mul_f32_e32 v136, v136, v170
	v_mul_f32_e32 v137, v137, v171
	v_mul_f32_e32 v138, v138, v168
	v_mul_f32_e32 v139, v139, v169
	v_exp_f32_e32 v168, v172
	v_exp_f32_e32 v169, v173
	v_exp_f32_e32 v170, v180
	v_exp_f32_e32 v171, v181
	v_add_f32_e32 v140, 1.0, v140
	v_add_f32_e32 v141, 1.0, v141
	v_add_f32_e32 v142, 1.0, v142
	v_add_f32_e32 v143, 1.0, v143
	v_rcp_f32_e32 v140, v140
	v_rcp_f32_e32 v142, v142
	v_rcp_f32_e32 v141, v141
	v_rcp_f32_e32 v143, v143
	v_add_f32_e32 v168, 1.0, v168
	v_add_f32_e32 v169, 1.0, v169
	v_add_f32_e32 v170, 1.0, v170
	v_add_f32_e32 v171, 1.0, v171
	v_rcp_f32_e32 v168, v168
	v_rcp_f32_e32 v170, v170
	v_rcp_f32_e32 v169, v169
	v_rcp_f32_e32 v171, v171
	v_mul_f32_e32 v132, v132, v140
	v_mul_f32_e32 v133, v133, v141
	v_mul_f32_e32 v136, v136, v142
	v_mul_f32_e32 v137, v137, v143
	v_cvt_pk_fp8_f32 v174, v132, v133
	v_cvt_pk_fp8_f32 v175, v136, v137
	v_mul_f32_e32 v132, v134, v168
	v_mul_f32_e32 v133, v135, v169
	v_mul_f32_e32 v134, v138, v170
	v_mul_f32_e32 v135, v139, v171
	v_cvt_pk_fp8_f32 v174, v132, v133 op_sel:[0,0,1]
	v_cvt_pk_fp8_f32 v175, v134, v135 op_sel:[0,0,1]
	v_lshl_add_u64 v[132:133], v[166:167], 0, v[128:129]
	v_or_b32_e32 v136, 32, v158
	global_store_dwordx2 v[132:133], v[174:175], off
	v_mov_b32_e32 v134, 0
	v_mov_b32_e32 v135, 0
	v_mad_i64_i32 v[138:139], s[28:29], v176, s62, v[130:131]
	v_ashrrev_i32_e32 v137, 31, v136
	v_cvt_f32_i32_e32 v56, v56
	v_cvt_f32_i32_e32 v63, v63
	v_cvt_f32_i32_e32 v62, v62
	v_cvt_f32_i32_e32 v59, v59
	v_cvt_f32_i32_e32 v58, v58
	v_cvt_f32_i32_e32 v49, v49
	v_cvt_f32_i32_e32 v48, v48
	v_cvt_f32_i32_e32 v51, v51
	v_cvt_f32_i32_e32 v50, v50
	v_cvt_f32_i32_e32 v53, v53
	v_cvt_f32_i32_e32 v52, v52
	v_cvt_f32_i32_e32 v55, v55
	v_cvt_f32_i32_e32 v54, v54
	v_cvt_f32_i32_e32 v45, v45
	v_cvt_f32_i32_e32 v44, v44
	v_cvt_f32_i32_e32 v41, v41
	v_cvt_f32_i32_e32 v40, v40
	v_cvt_f32_i32_e32 v47, v47
	v_cvt_f32_i32_e32 v46, v46
	v_cvt_f32_i32_e32 v43, v43
	v_cvt_f32_i32_e32 v42, v42
	v_cvt_f32_i32_e32 v33, v33
	v_cvt_f32_i32_e32 v32, v32
	v_cvt_f32_i32_e32 v35, v35
	v_cvt_f32_i32_e32 v34, v34
	v_cvt_f32_i32_e32 v37, v37
	v_cvt_f32_i32_e32 v36, v36
	v_cvt_f32_i32_e32 v39, v39
	v_cvt_f32_i32_e32 v38, v38
	v_cvt_f32_i32_e32 v29, v29
	v_cvt_f32_i32_e32 v28, v28
	v_cvt_f32_i32_e32 v25, v25
	v_cvt_f32_i32_e32 v24, v24
	v_cvt_f32_i32_e32 v31, v31
	v_cvt_f32_i32_e32 v30, v30
	v_cvt_f32_i32_e32 v27, v27
	v_cvt_f32_i32_e32 v26, v26
	v_cvt_f32_i32_e32 v17, v17
	v_cvt_f32_i32_e32 v16, v16
	v_cvt_f32_i32_e32 v19, v19
	v_cvt_f32_i32_e32 v18, v18
	v_cvt_f32_i32_e32 v21, v21
	v_cvt_f32_i32_e32 v20, v20
	v_cvt_f32_i32_e32 v23, v23
	v_cvt_f32_i32_e32 v22, v22
	v_cvt_f32_i32_e32 v13, v13
	v_cvt_f32_i32_e32 v12, v12
	v_cvt_f32_i32_e32 v9, v9
	v_cvt_f32_i32_e32 v8, v8
	v_cvt_f32_i32_e32 v15, v15
	v_cvt_f32_i32_e32 v14, v14
	v_cvt_f32_i32_e32 v11, v11
	v_cvt_f32_i32_e32 v10, v10
	v_cvt_f32_i32_e32 v1, v1
	v_cvt_f32_i32_e32 v0, v0
	v_cvt_f32_i32_e32 v3, v3
	v_cvt_f32_i32_e32 v2, v2
	v_cvt_f32_i32_e32 v5, v5
	v_cvt_f32_i32_e32 v4, v4
	v_cvt_f32_i32_e32 v7, v7
	v_cvt_f32_i32_e32 v6, v6
	s_andn2_b64 vcc, exec, s[0:1]
	s_mov_b64 s[0:1], -1
	s_waitcnt vmcnt(7)
	v_mul_f32_e32 v142, v88, v194
	v_mul_f32_e32 v143, v89, v194
	v_mul_f32_e32 v168, v84, v194
	v_mul_f32_e32 v169, v85, v194
	v_mul_f32_e32 v140, v90, v194
	v_mul_f32_e32 v141, v91, v194
	v_mul_f32_e32 v166, v86, v194
	v_mul_f32_e32 v167, v87, v194
	v_mul_f32_e32 v170, v80, v194
	v_mul_f32_e32 v171, v81, v194
	v_mul_f32_e32 v172, v82, v194
	v_mul_f32_e32 v173, v83, v194
	v_mul_f32_e32 v174, v76, v194
	v_mul_f32_e32 v175, v77, v194
	v_mul_f32_e32 v132, v78, v194
	v_mul_f32_e32 v133, v79, v194
	v_mul_f32_e32 v124, v142, v124
	v_mul_f32_e32 v125, v143, v125
	v_mul_f32_e32 v120, v168, v120
	v_mul_f32_e32 v121, v169, v121
	v_mul_f32_e32 v126, v140, v126
	v_mul_f32_e32 v127, v141, v127
	v_mul_f32_e32 v122, v166, v122
	v_mul_f32_e32 v123, v167, v123
	v_mul_f32_e32 v114, v132, v114
	v_mul_f32_e32 v115, v133, v115
	v_mul_f32_e32 v112, v174, v112
	v_mul_f32_e32 v113, v175, v113
	v_mul_f32_e32 v140, s14, v124
	v_mul_f32_e32 v141, s14, v125
	v_mul_f32_e32 v166, s14, v120
	v_mul_f32_e32 v167, s14, v121
	v_mul_f32_e32 v142, s14, v122
	v_mul_f32_e32 v143, s14, v123
	v_mul_f32_e32 v112, v120, v112
	v_mul_f32_e32 v113, v121, v113
	v_mul_f32_e32 v114, v122, v114
	v_mul_f32_e32 v115, v123, v115
	v_exp_f32_e32 v120, v140
	v_exp_f32_e32 v122, v166
	v_exp_f32_e32 v121, v141
	v_exp_f32_e32 v123, v167
	v_mul_f32_e32 v118, v172, v118
	v_mul_f32_e32 v119, v173, v119
	v_mul_f32_e32 v116, v170, v116
	v_mul_f32_e32 v117, v171, v117
	v_mul_f32_e32 v132, s14, v126
	v_mul_f32_e32 v133, s14, v127
	v_mul_f32_e32 v116, v124, v116
	v_mul_f32_e32 v117, v125, v117
	v_mul_f32_e32 v118, v126, v118
	v_mul_f32_e32 v119, v127, v119
	v_exp_f32_e32 v124, v132
	v_exp_f32_e32 v125, v133
	v_exp_f32_e32 v126, v142
	v_exp_f32_e32 v127, v143
	v_add_f32_e32 v120, 1.0, v120
	v_add_f32_e32 v121, 1.0, v121
	v_add_f32_e32 v122, 1.0, v122
	v_add_f32_e32 v123, 1.0, v123
	v_rcp_f32_e32 v120, v120
	v_rcp_f32_e32 v122, v122
	v_rcp_f32_e32 v121, v121
	v_rcp_f32_e32 v123, v123
	v_add_f32_e32 v124, 1.0, v124
	v_add_f32_e32 v125, 1.0, v125
	v_add_f32_e32 v126, 1.0, v126
	v_add_f32_e32 v127, 1.0, v127
	v_rcp_f32_e32 v124, v124
	v_rcp_f32_e32 v126, v126
	v_rcp_f32_e32 v125, v125
	v_rcp_f32_e32 v127, v127
	v_mul_f32_e32 v116, v116, v120
	v_mul_f32_e32 v117, v117, v121
	v_mul_f32_e32 v112, v112, v122
	v_mul_f32_e32 v113, v113, v123
	v_cvt_pk_fp8_f32 v134, v116, v117
	v_cvt_pk_fp8_f32 v135, v112, v113
	v_mul_f32_e32 v112, v118, v124
	v_mul_f32_e32 v113, v119, v125
	v_mul_f32_e32 v114, v114, v126
	v_mul_f32_e32 v115, v115, v127
	v_cvt_pk_fp8_f32 v134, v112, v113 op_sel:[0,0,1]
	v_cvt_pk_fp8_f32 v135, v114, v115 op_sel:[0,0,1]
	v_lshl_add_u64 v[112:113], v[138:139], 0, v[128:129]
	v_mad_i64_i32 v[118:119], s[28:29], v136, s62, v[130:131]
	global_store_dwordx2 v[112:113], v[134:135], off
	v_mov_b32_e32 v114, 0
	v_mov_b32_e32 v115, 0
	v_or_b32_e32 v116, 48, v158
	v_ashrrev_i32_e32 v117, 31, v116
	s_waitcnt vmcnt(7)
	v_mul_f32_e32 v122, v88, v196
	v_mul_f32_e32 v123, v89, v196
	v_mul_f32_e32 v126, v84, v196
	v_mul_f32_e32 v127, v85, v196
	v_mul_f32_e32 v120, v90, v196
	v_mul_f32_e32 v121, v91, v196
	v_mul_f32_e32 v124, v86, v196
	v_mul_f32_e32 v125, v87, v196
	v_mul_f32_e32 v132, v80, v196
	v_mul_f32_e32 v133, v81, v196
	v_mul_f32_e32 v134, v82, v196
	v_mul_f32_e32 v135, v83, v196
	v_mul_f32_e32 v136, v76, v196
	v_mul_f32_e32 v137, v77, v196
	v_mul_f32_e32 v112, v78, v196
	v_mul_f32_e32 v113, v79, v196
	v_mul_f32_e32 v108, v122, v108
	v_mul_f32_e32 v109, v123, v109
	v_mul_f32_e32 v104, v126, v104
	v_mul_f32_e32 v105, v127, v105
	v_mul_f32_e32 v110, v120, v110
	v_mul_f32_e32 v111, v121, v111
	v_mul_f32_e32 v106, v124, v106
	v_mul_f32_e32 v107, v125, v107
	v_mul_f32_e32 v98, v112, v98
	v_mul_f32_e32 v99, v113, v99
	v_mul_f32_e32 v96, v136, v96
	v_mul_f32_e32 v97, v137, v97
	v_mul_f32_e32 v120, s14, v108
	v_mul_f32_e32 v121, s14, v109
	v_mul_f32_e32 v124, s14, v104
	v_mul_f32_e32 v125, s14, v105
	v_mul_f32_e32 v122, s14, v106
	v_mul_f32_e32 v123, s14, v107
	v_mul_f32_e32 v96, v104, v96
	v_mul_f32_e32 v97, v105, v97
	v_mul_f32_e32 v98, v106, v98
	v_mul_f32_e32 v99, v107, v99
	v_exp_f32_e32 v104, v120
	v_exp_f32_e32 v106, v124
	v_exp_f32_e32 v105, v121
	v_exp_f32_e32 v107, v125
	v_mul_f32_e32 v102, v134, v102
	v_mul_f32_e32 v103, v135, v103
	v_mul_f32_e32 v100, v132, v100
	v_mul_f32_e32 v101, v133, v101
	v_mul_f32_e32 v112, s14, v110
	v_mul_f32_e32 v113, s14, v111
	v_mul_f32_e32 v100, v108, v100
	v_mul_f32_e32 v101, v109, v101
	v_mul_f32_e32 v102, v110, v102
	v_mul_f32_e32 v103, v111, v103
	v_exp_f32_e32 v108, v112
	v_exp_f32_e32 v109, v113
	v_exp_f32_e32 v110, v122
	v_exp_f32_e32 v111, v123
	v_add_f32_e32 v104, 1.0, v104
	v_add_f32_e32 v105, 1.0, v105
	v_add_f32_e32 v106, 1.0, v106
	v_add_f32_e32 v107, 1.0, v107
	v_rcp_f32_e32 v104, v104
	v_rcp_f32_e32 v106, v106
	v_rcp_f32_e32 v105, v105
	v_rcp_f32_e32 v107, v107
	v_add_f32_e32 v108, 1.0, v108
	v_add_f32_e32 v109, 1.0, v109
	v_add_f32_e32 v110, 1.0, v110
	v_add_f32_e32 v111, 1.0, v111
	v_rcp_f32_e32 v108, v108
	v_rcp_f32_e32 v110, v110
	v_rcp_f32_e32 v109, v109
	v_rcp_f32_e32 v111, v111
	v_mul_f32_e32 v100, v100, v104
	v_mul_f32_e32 v101, v101, v105
	v_mul_f32_e32 v96, v96, v106
	v_mul_f32_e32 v97, v97, v107
	v_cvt_pk_fp8_f32 v114, v100, v101
	v_cvt_pk_fp8_f32 v115, v96, v97
	v_mul_f32_e32 v96, v102, v108
	v_mul_f32_e32 v97, v103, v109
	v_mul_f32_e32 v98, v98, v110
	v_mul_f32_e32 v99, v99, v111
	v_cvt_pk_fp8_f32 v114, v96, v97 op_sel:[0,0,1]
	v_cvt_pk_fp8_f32 v115, v98, v99 op_sel:[0,0,1]
	v_lshl_add_u64 v[96:97], v[118:119], 0, v[128:129]
	global_store_dwordx2 v[96:97], v[114:115], off
	v_mov_b32_e32 v98, 0
	v_mov_b32_e32 v99, 0
	s_waitcnt vmcnt(7)
	v_mul_f32_e32 v102, v88, v198
	v_mul_f32_e32 v103, v89, v198
	v_mul_f32_e32 v106, v84, v198
	v_mul_f32_e32 v107, v85, v198
	v_mul_f32_e32 v100, v90, v198
	v_mul_f32_e32 v101, v91, v198
	v_mul_f32_e32 v104, v86, v198
	v_mul_f32_e32 v105, v87, v198
	v_mul_f32_e32 v108, v80, v198
	v_mul_f32_e32 v109, v81, v198
	v_mul_f32_e32 v110, v82, v198
	v_mul_f32_e32 v111, v83, v198
	v_mul_f32_e32 v112, v76, v198
	v_mul_f32_e32 v113, v77, v198
	v_mul_f32_e32 v96, v78, v198
	v_mul_f32_e32 v97, v79, v198
	v_mul_f32_e32 v92, v102, v92
	v_mul_f32_e32 v93, v103, v93
	v_mul_f32_e32 v72, v106, v72
	v_mul_f32_e32 v73, v107, v73
	v_mul_f32_e32 v94, v100, v94
	v_mul_f32_e32 v95, v101, v95
	v_mul_f32_e32 v74, v104, v74
	v_mul_f32_e32 v75, v105, v75
	v_mul_f32_e32 v66, v96, v66
	v_mul_f32_e32 v67, v97, v67
	v_mul_f32_e32 v64, v112, v64
	v_mul_f32_e32 v65, v113, v65
	v_mul_f32_e32 v100, s14, v92
	v_mul_f32_e32 v101, s14, v93
	v_mul_f32_e32 v104, s14, v72
	v_mul_f32_e32 v105, s14, v73
	v_mul_f32_e32 v102, s14, v74
	v_mul_f32_e32 v103, s14, v75
	v_mul_f32_e32 v64, v72, v64
	v_mul_f32_e32 v65, v73, v65
	v_mul_f32_e32 v66, v74, v66
	v_mul_f32_e32 v67, v75, v67
	v_exp_f32_e32 v72, v100
	v_exp_f32_e32 v74, v104
	v_exp_f32_e32 v73, v101
	v_exp_f32_e32 v75, v105
	v_mul_f32_e32 v70, v110, v70
	v_mul_f32_e32 v71, v111, v71
	v_mul_f32_e32 v68, v108, v68
	v_mul_f32_e32 v69, v109, v69
	v_mul_f32_e32 v96, s14, v94
	v_mul_f32_e32 v97, s14, v95
	v_mul_f32_e32 v68, v92, v68
	v_mul_f32_e32 v69, v93, v69
	v_mul_f32_e32 v70, v94, v70
	v_mul_f32_e32 v71, v95, v71
	v_exp_f32_e32 v92, v96
	v_exp_f32_e32 v93, v97
	v_exp_f32_e32 v94, v102
	v_exp_f32_e32 v95, v103
	v_add_f32_e32 v72, 1.0, v72
	v_add_f32_e32 v73, 1.0, v73
	v_add_f32_e32 v74, 1.0, v74
	v_add_f32_e32 v75, 1.0, v75
	v_rcp_f32_e32 v72, v72
	v_rcp_f32_e32 v74, v74
	v_rcp_f32_e32 v73, v73
	v_rcp_f32_e32 v75, v75
	v_add_f32_e32 v92, 1.0, v92
	v_add_f32_e32 v93, 1.0, v93
	v_add_f32_e32 v94, 1.0, v94
	v_add_f32_e32 v95, 1.0, v95
	v_rcp_f32_e32 v92, v92
	v_rcp_f32_e32 v94, v94
	v_rcp_f32_e32 v93, v93
	v_rcp_f32_e32 v95, v95
	v_mul_f32_e32 v68, v68, v72
	v_mul_f32_e32 v69, v69, v73
	v_mul_f32_e32 v64, v64, v74
	v_mul_f32_e32 v65, v65, v75
	v_cvt_pk_fp8_f32 v98, v68, v69
	v_cvt_pk_fp8_f32 v99, v64, v65
	v_mul_f32_e32 v64, v70, v92
	v_mul_f32_e32 v65, v71, v93
	v_mul_f32_e32 v66, v66, v94
	v_mul_f32_e32 v67, v67, v95
	v_cvt_pk_fp8_f32 v98, v64, v65 op_sel:[0,0,1]
	v_cvt_pk_fp8_f32 v99, v66, v67 op_sel:[0,0,1]
	v_mad_i64_i32 v[64:65], s[28:29], v116, s62, v[130:131]
	v_lshl_add_u64 v[64:65], v[64:65], 0, v[128:129]
	global_store_dwordx2 v[64:65], v[98:99], off
	v_mov_b32_e32 v66, 0
	v_mov_b32_e32 v67, 0
	v_add_u32_e32 v98, 0x80, v158
	s_waitcnt vmcnt(7)
	v_mul_f32_e32 v70, v88, v200
	v_mul_f32_e32 v71, v89, v200
	v_mul_f32_e32 v74, v84, v200
	v_mul_f32_e32 v75, v85, v200
	v_mul_f32_e32 v68, v90, v200
	v_mul_f32_e32 v69, v91, v200
	v_mul_f32_e32 v72, v86, v200
	v_mul_f32_e32 v73, v87, v200
	v_mul_f32_e32 v92, v80, v200
	v_mul_f32_e32 v93, v81, v200
	v_mul_f32_e32 v94, v82, v200
	v_mul_f32_e32 v95, v83, v200
	v_mul_f32_e32 v96, v76, v200
	v_mul_f32_e32 v97, v77, v200
	v_mul_f32_e32 v64, v78, v200
	v_mul_f32_e32 v65, v79, v200
	v_mul_f32_e32 v60, v70, v60
	v_mul_f32_e32 v61, v71, v61
	v_mul_f32_e32 v56, v74, v56
	v_mul_f32_e32 v57, v75, v57
	v_mul_f32_e32 v62, v68, v62
	v_mul_f32_e32 v63, v69, v63
	v_mul_f32_e32 v58, v72, v58
	v_mul_f32_e32 v59, v73, v59
	v_mul_f32_e32 v50, v64, v50
	v_mul_f32_e32 v51, v65, v51
	v_mul_f32_e32 v48, v96, v48
	v_mul_f32_e32 v49, v97, v49
	v_mul_f32_e32 v68, s14, v60
	v_mul_f32_e32 v69, s14, v61
	v_mul_f32_e32 v72, s14, v56
	v_mul_f32_e32 v73, s14, v57
	v_mul_f32_e32 v70, s14, v58
	v_mul_f32_e32 v71, s14, v59
	v_mul_f32_e32 v48, v56, v48
	v_mul_f32_e32 v49, v57, v49
	v_mul_f32_e32 v50, v58, v50
	v_mul_f32_e32 v51, v59, v51
	v_exp_f32_e32 v56, v68
	v_exp_f32_e32 v58, v72
	v_exp_f32_e32 v57, v69
	v_exp_f32_e32 v59, v73
	v_mul_f32_e32 v54, v94, v54
	v_mul_f32_e32 v55, v95, v55
	v_mul_f32_e32 v52, v92, v52
	v_mul_f32_e32 v53, v93, v53
	v_mul_f32_e32 v64, s14, v62
	v_mul_f32_e32 v65, s14, v63
	v_mul_f32_e32 v52, v60, v52
	v_mul_f32_e32 v53, v61, v53
	v_mul_f32_e32 v54, v62, v54
	v_mul_f32_e32 v55, v63, v55
	v_exp_f32_e32 v60, v64
	v_exp_f32_e32 v61, v65
	v_exp_f32_e32 v62, v70
	v_exp_f32_e32 v63, v71
	v_add_f32_e32 v56, 1.0, v56
	v_add_f32_e32 v57, 1.0, v57
	v_add_f32_e32 v58, 1.0, v58
	v_add_f32_e32 v59, 1.0, v59
	v_rcp_f32_e32 v56, v56
	v_rcp_f32_e32 v58, v58
	v_rcp_f32_e32 v57, v57
	v_rcp_f32_e32 v59, v59
	v_add_f32_e32 v60, 1.0, v60
	v_add_f32_e32 v61, 1.0, v61
	v_add_f32_e32 v62, 1.0, v62
	v_add_f32_e32 v63, 1.0, v63
	v_rcp_f32_e32 v60, v60
	v_rcp_f32_e32 v62, v62
	v_rcp_f32_e32 v61, v61
	v_rcp_f32_e32 v63, v63
	v_mul_f32_e32 v52, v52, v56
	v_mul_f32_e32 v53, v53, v57
	v_mul_f32_e32 v48, v48, v58
	v_mul_f32_e32 v49, v49, v59
	v_cvt_pk_fp8_f32 v66, v52, v53
	v_cvt_pk_fp8_f32 v67, v48, v49
	v_mul_f32_e32 v48, v54, v60
	v_mul_f32_e32 v49, v55, v61
	v_mul_f32_e32 v50, v50, v62
	v_mul_f32_e32 v51, v51, v63
	v_cvt_pk_fp8_f32 v66, v48, v49 op_sel:[0,0,1]
	v_cvt_pk_fp8_f32 v67, v50, v51 op_sel:[0,0,1]
	v_mad_i64_i32 v[48:49], s[28:29], v98, s62, v[130:131]
	v_lshl_add_u64 v[48:49], v[48:49], 0, v[128:129]
	global_store_dwordx2 v[48:49], v[66:67], off
	v_mov_b32_e32 v50, 0
	v_mov_b32_e32 v51, 0
	v_add_u32_e32 v66, 0x90, v158
	s_waitcnt vmcnt(7)
	v_mul_f32_e32 v54, v88, v202
	v_mul_f32_e32 v55, v89, v202
	v_mul_f32_e32 v58, v84, v202
	v_mul_f32_e32 v59, v85, v202
	v_mul_f32_e32 v52, v90, v202
	v_mul_f32_e32 v53, v91, v202
	v_mul_f32_e32 v56, v86, v202
	v_mul_f32_e32 v57, v87, v202
	v_mul_f32_e32 v60, v80, v202
	v_mul_f32_e32 v61, v81, v202
	v_mul_f32_e32 v62, v82, v202
	v_mul_f32_e32 v63, v83, v202
	v_mul_f32_e32 v64, v76, v202
	v_mul_f32_e32 v65, v77, v202
	v_mul_f32_e32 v48, v78, v202
	v_mul_f32_e32 v49, v79, v202
	v_mul_f32_e32 v44, v54, v44
	v_mul_f32_e32 v45, v55, v45
	v_mul_f32_e32 v40, v58, v40
	v_mul_f32_e32 v41, v59, v41
	v_mul_f32_e32 v46, v52, v46
	v_mul_f32_e32 v47, v53, v47
	v_mul_f32_e32 v42, v56, v42
	v_mul_f32_e32 v43, v57, v43
	v_mul_f32_e32 v34, v48, v34
	v_mul_f32_e32 v35, v49, v35
	v_mul_f32_e32 v32, v64, v32
	v_mul_f32_e32 v33, v65, v33
	v_mul_f32_e32 v52, s14, v44
	v_mul_f32_e32 v53, s14, v45
	v_mul_f32_e32 v56, s14, v40
	v_mul_f32_e32 v57, s14, v41
	v_mul_f32_e32 v54, s14, v42
	v_mul_f32_e32 v55, s14, v43
	v_mul_f32_e32 v32, v40, v32
	v_mul_f32_e32 v33, v41, v33
	v_mul_f32_e32 v34, v42, v34
	v_mul_f32_e32 v35, v43, v35
	v_exp_f32_e32 v40, v52
	v_exp_f32_e32 v42, v56
	v_exp_f32_e32 v41, v53
	v_exp_f32_e32 v43, v57
	v_mul_f32_e32 v38, v62, v38
	v_mul_f32_e32 v39, v63, v39
	v_mul_f32_e32 v36, v60, v36
	v_mul_f32_e32 v37, v61, v37
	v_mul_f32_e32 v48, s14, v46
	v_mul_f32_e32 v49, s14, v47
	v_mul_f32_e32 v36, v44, v36
	v_mul_f32_e32 v37, v45, v37
	v_mul_f32_e32 v38, v46, v38
	v_mul_f32_e32 v39, v47, v39
	v_exp_f32_e32 v44, v48
	v_exp_f32_e32 v45, v49
	v_exp_f32_e32 v46, v54
	v_exp_f32_e32 v47, v55
	v_add_f32_e32 v40, 1.0, v40
	v_add_f32_e32 v41, 1.0, v41
	v_add_f32_e32 v42, 1.0, v42
	v_add_f32_e32 v43, 1.0, v43
	v_rcp_f32_e32 v40, v40
	v_rcp_f32_e32 v42, v42
	v_rcp_f32_e32 v41, v41
	v_rcp_f32_e32 v43, v43
	v_add_f32_e32 v44, 1.0, v44
	v_add_f32_e32 v45, 1.0, v45
	v_add_f32_e32 v46, 1.0, v46
	v_add_f32_e32 v47, 1.0, v47
	v_rcp_f32_e32 v44, v44
	v_rcp_f32_e32 v46, v46
	v_rcp_f32_e32 v45, v45
	v_rcp_f32_e32 v47, v47
	v_mul_f32_e32 v36, v36, v40
	v_mul_f32_e32 v37, v37, v41
	v_mul_f32_e32 v32, v32, v42
	v_mul_f32_e32 v33, v33, v43
	v_cvt_pk_fp8_f32 v50, v36, v37
	v_cvt_pk_fp8_f32 v51, v32, v33
	v_mul_f32_e32 v32, v38, v44
	v_mul_f32_e32 v33, v39, v45
	v_mul_f32_e32 v34, v34, v46
	v_mul_f32_e32 v35, v35, v47
	v_cvt_pk_fp8_f32 v50, v32, v33 op_sel:[0,0,1]
	v_cvt_pk_fp8_f32 v51, v34, v35 op_sel:[0,0,1]
	v_mad_i64_i32 v[32:33], s[28:29], v66, s62, v[130:131]
	v_lshl_add_u64 v[32:33], v[32:33], 0, v[128:129]
	global_store_dwordx2 v[32:33], v[50:51], off
	v_mov_b32_e32 v34, 0
	v_mov_b32_e32 v35, 0
	v_add_u32_e32 v50, 0xa0, v158
	s_waitcnt vmcnt(7)
	v_mul_f32_e32 v38, v88, v204
	v_mul_f32_e32 v39, v89, v204
	v_mul_f32_e32 v42, v84, v204
	v_mul_f32_e32 v43, v85, v204
	v_mul_f32_e32 v36, v90, v204
	v_mul_f32_e32 v37, v91, v204
	v_mul_f32_e32 v40, v86, v204
	v_mul_f32_e32 v41, v87, v204
	v_mul_f32_e32 v44, v80, v204
	v_mul_f32_e32 v45, v81, v204
	v_mul_f32_e32 v46, v82, v204
	v_mul_f32_e32 v47, v83, v204
	v_mul_f32_e32 v48, v76, v204
	v_mul_f32_e32 v49, v77, v204
	v_mul_f32_e32 v32, v78, v204
	v_mul_f32_e32 v33, v79, v204
	v_mul_f32_e32 v28, v38, v28
	v_mul_f32_e32 v29, v39, v29
	v_mul_f32_e32 v24, v42, v24
	v_mul_f32_e32 v25, v43, v25
	v_mul_f32_e32 v30, v36, v30
	v_mul_f32_e32 v31, v37, v31
	v_mul_f32_e32 v26, v40, v26
	v_mul_f32_e32 v27, v41, v27
	v_mul_f32_e32 v18, v32, v18
	v_mul_f32_e32 v19, v33, v19
	v_mul_f32_e32 v16, v48, v16
	v_mul_f32_e32 v17, v49, v17
	v_mul_f32_e32 v36, s14, v28
	v_mul_f32_e32 v37, s14, v29
	v_mul_f32_e32 v40, s14, v24
	v_mul_f32_e32 v41, s14, v25
	v_mul_f32_e32 v38, s14, v26
	v_mul_f32_e32 v39, s14, v27
	v_mul_f32_e32 v16, v24, v16
	v_mul_f32_e32 v17, v25, v17
	v_mul_f32_e32 v18, v26, v18
	v_mul_f32_e32 v19, v27, v19
	v_exp_f32_e32 v24, v36
	v_exp_f32_e32 v26, v40
	v_exp_f32_e32 v25, v37
	v_exp_f32_e32 v27, v41
	v_mul_f32_e32 v22, v46, v22
	v_mul_f32_e32 v23, v47, v23
	v_mul_f32_e32 v20, v44, v20
	v_mul_f32_e32 v21, v45, v21
	v_mul_f32_e32 v32, s14, v30
	v_mul_f32_e32 v33, s14, v31
	v_mul_f32_e32 v20, v28, v20
	v_mul_f32_e32 v21, v29, v21
	v_mul_f32_e32 v22, v30, v22
	v_mul_f32_e32 v23, v31, v23
	v_exp_f32_e32 v28, v32
	v_exp_f32_e32 v29, v33
	v_exp_f32_e32 v30, v38
	v_exp_f32_e32 v31, v39
	v_add_f32_e32 v24, 1.0, v24
	v_add_f32_e32 v25, 1.0, v25
	v_add_f32_e32 v26, 1.0, v26
	v_add_f32_e32 v27, 1.0, v27
	v_rcp_f32_e32 v24, v24
	v_rcp_f32_e32 v26, v26
	v_rcp_f32_e32 v25, v25
	v_rcp_f32_e32 v27, v27
	v_add_f32_e32 v28, 1.0, v28
	v_add_f32_e32 v29, 1.0, v29
	v_add_f32_e32 v30, 1.0, v30
	v_add_f32_e32 v31, 1.0, v31
	v_rcp_f32_e32 v28, v28
	v_rcp_f32_e32 v30, v30
	v_rcp_f32_e32 v29, v29
	v_rcp_f32_e32 v31, v31
	v_mul_f32_e32 v20, v20, v24
	v_mul_f32_e32 v21, v21, v25
	v_mul_f32_e32 v16, v16, v26
	v_mul_f32_e32 v17, v17, v27
	v_cvt_pk_fp8_f32 v34, v20, v21
	v_cvt_pk_fp8_f32 v35, v16, v17
	v_mul_f32_e32 v16, v22, v28
	v_mul_f32_e32 v17, v23, v29
	v_mul_f32_e32 v18, v18, v30
	v_mul_f32_e32 v19, v19, v31
	v_cvt_pk_fp8_f32 v34, v16, v17 op_sel:[0,0,1]
	v_cvt_pk_fp8_f32 v35, v18, v19 op_sel:[0,0,1]
	v_mad_i64_i32 v[16:17], s[28:29], v50, s62, v[130:131]
	v_lshl_add_u64 v[16:17], v[16:17], 0, v[128:129]
	global_store_dwordx2 v[16:17], v[34:35], off
	v_mov_b32_e32 v18, 0
	v_mov_b32_e32 v19, 0
	v_add_u32_e32 v34, 0xb0, v158
	s_waitcnt vmcnt(7)
	v_mul_f32_e32 v22, v88, v206
	v_mul_f32_e32 v23, v89, v206
	v_mul_f32_e32 v26, v84, v206
	v_mul_f32_e32 v27, v85, v206
	v_mul_f32_e32 v20, v90, v206
	v_mul_f32_e32 v21, v91, v206
	v_mul_f32_e32 v24, v86, v206
	v_mul_f32_e32 v25, v87, v206
	v_mul_f32_e32 v28, v80, v206
	v_mul_f32_e32 v29, v81, v206
	v_mul_f32_e32 v30, v82, v206
	v_mul_f32_e32 v31, v83, v206
	v_mul_f32_e32 v32, v76, v206
	v_mul_f32_e32 v33, v77, v206
	v_mul_f32_e32 v16, v78, v206
	v_mul_f32_e32 v17, v79, v206
	v_mul_f32_e32 v12, v22, v12
	v_mul_f32_e32 v13, v23, v13
	v_mul_f32_e32 v8, v26, v8
	v_mul_f32_e32 v9, v27, v9
	v_mul_f32_e32 v14, v20, v14
	v_mul_f32_e32 v15, v21, v15
	v_mul_f32_e32 v10, v24, v10
	v_mul_f32_e32 v11, v25, v11
	v_mul_f32_e32 v2, v16, v2
	v_mul_f32_e32 v3, v17, v3
	v_mul_f32_e32 v0, v32, v0
	v_mul_f32_e32 v1, v33, v1
	v_mul_f32_e32 v20, s14, v12
	v_mul_f32_e32 v21, s14, v13
	v_mul_f32_e32 v24, s14, v8
	v_mul_f32_e32 v25, s14, v9
	v_mul_f32_e32 v22, s14, v10
	v_mul_f32_e32 v23, s14, v11
	v_mul_f32_e32 v0, v8, v0
	v_mul_f32_e32 v1, v9, v1
	v_mul_f32_e32 v2, v10, v2
	v_mul_f32_e32 v3, v11, v3
	v_exp_f32_e32 v8, v20
	v_exp_f32_e32 v10, v24
	v_exp_f32_e32 v9, v21
	v_exp_f32_e32 v11, v25
	v_mul_f32_e32 v6, v30, v6
	v_mul_f32_e32 v7, v31, v7
	v_mul_f32_e32 v4, v28, v4
	v_mul_f32_e32 v5, v29, v5
	v_mul_f32_e32 v16, s14, v14
	v_mul_f32_e32 v17, s14, v15
	v_mul_f32_e32 v4, v12, v4
	v_mul_f32_e32 v5, v13, v5
	v_mul_f32_e32 v6, v14, v6
	v_mul_f32_e32 v7, v15, v7
	v_exp_f32_e32 v12, v16
	v_exp_f32_e32 v13, v17
	v_exp_f32_e32 v14, v22
	v_exp_f32_e32 v15, v23
	v_add_f32_e32 v8, 1.0, v8
	v_add_f32_e32 v9, 1.0, v9
	v_add_f32_e32 v10, 1.0, v10
	v_add_f32_e32 v11, 1.0, v11
	v_rcp_f32_e32 v8, v8
	v_rcp_f32_e32 v10, v10
	v_rcp_f32_e32 v9, v9
	v_rcp_f32_e32 v11, v11
	v_add_f32_e32 v12, 1.0, v12
	v_add_f32_e32 v13, 1.0, v13
	v_add_f32_e32 v14, 1.0, v14
	v_add_f32_e32 v15, 1.0, v15
	v_rcp_f32_e32 v12, v12
	v_rcp_f32_e32 v14, v14
	v_rcp_f32_e32 v13, v13
	v_rcp_f32_e32 v15, v15
	v_mul_f32_e32 v4, v4, v8
	v_mul_f32_e32 v5, v5, v9
	v_mul_f32_e32 v0, v0, v10
	v_mul_f32_e32 v1, v1, v11
	v_cvt_pk_fp8_f32 v18, v4, v5
	v_cvt_pk_fp8_f32 v19, v0, v1
	v_mul_f32_e32 v0, v6, v12
	v_mul_f32_e32 v1, v7, v13
	v_mul_f32_e32 v2, v2, v14
	v_mul_f32_e32 v3, v3, v15
	v_cvt_pk_fp8_f32 v18, v0, v1 op_sel:[0,0,1]
	v_cvt_pk_fp8_f32 v19, v2, v3 op_sel:[0,0,1]
	v_mad_i64_i32 v[0:1], s[28:29], v34, s62, v[130:131]
	v_lshl_add_u64 v[0:1], v[0:1], 0, v[128:129]
	global_store_dwordx2 v[0:1], v[18:19], off
	s_cbranch_vccnz .LBB0_1844
	s_andn2_b64 vcc, exec, s[4:5]
	s_cbranch_vccnz .LBB0_1843
	s_barrier
	s_branch .LBB0_1843
